# speedup vs baseline: 1.0207x; 1.0026x over previous
_Z11attn_kernelPKDF16_S0_S0_PKjPf:
	s_and_b32 s27, s2, 7
	s_lshr_b32 s3, s2, 3
	s_lshr_b32 s12, s2, 6
	v_readfirstlane_b32 s23, v0
	s_mov_b32 s13, 0
	s_lshl_b32 s2, s2, 5
	s_load_dwordx8 s[4:11], s[0:1], 0x0
	s_and_b32 s28, s3, 0x1ffffff8
	s_lshr_b32 s20, s23, 6
	s_lshl_b64 s[14:15], s[12:13], 11
	s_and_b32 s2, s2, 0x700
	s_or_b32 s16, s28, s27
	s_or_b32 s2, s14, s2
	s_lshl_b32 s3, s20, 5
	s_add_u32 s2, s2, s3
	s_addc_u32 s3, s15, 0
	s_lshl_b64 s[14:15], s[2:3], 10
	s_waitcnt lgkmcnt(0)
	s_add_u32 s4, s4, s14
	s_addc_u32 s5, s5, s15
	s_lshl_b32 s12, s27, 7
	s_add_u32 s4, s4, s12
	s_mov_b32 s17, s13
	s_addc_u32 s5, s5, 0
	s_lshl_b64 s[12:13], s[16:17], 18
	s_add_u32 s14, s6, s12
	s_addc_u32 s15, s7, s13
	s_add_u32 s12, s8, s12
	s_addc_u32 s13, s9, s13
	s_lshl_b32 s22, s20, 10
	s_cmp_lg_u32 0, -1
	v_and_b32_e32 v1, 63, v0
	s_cselect_b32 s6, 0, 0
	v_lshl_or_b32 v189, v1, 4, s22
	s_add_i32 s24, s22, s6
	s_mov_b32 s6, m0
	s_mov_b32 m0, s24
	s_nop 0
	global_load_lds_dwordx4 v189, s[14:15]
	s_mov_b32 m0, s6
	v_bfe_u32 v18, v0, 5, 1
	s_add_i32 s25, s24, 0x6000
	s_mov_b32 s6, m0
	s_mov_b32 m0, s25
	s_nop 0
	global_load_lds_dwordx4 v189, s[12:13]
	s_mov_b32 m0, s6
	v_and_b32_e32 v181, 31, v0
	s_add_u32 s6, s14, 0x2000
	v_lshlrev_b32_e32 v184, 4, v18
	s_addc_u32 s7, s15, 0
	s_add_i32 s17, s24, 0x2000
	s_mov_b32 s18, m0
	s_mov_b32 m0, s17
	s_nop 0
	global_load_lds_dwordx4 v189, s[6:7]
	s_mov_b32 m0, s18
	v_lshl_or_b32 v2, v181, 10, v184
	global_load_dwordx4 v[124:127], v2, s[4:5]
	global_load_dwordx4 v[120:123], v2, s[4:5] offset:32
	global_load_dwordx4 v[116:119], v2, s[4:5] offset:64
	global_load_dwordx4 v[112:115], v2, s[4:5] offset:96
	v_lshlrev_b32_e32 v182, 10, v18
	v_lshlrev_b32_e32 v19, 4, v181
	v_add3_u32 v190, 0, v182, v19
	s_lshl_b32 s5, s16, 2
	s_load_dword s5, s[10:11], s5 offset:0x0
	s_mov_b32 s4, 0x42a20000
	v_mov_b32_e32 v2, 0
	v_mov_b32_e32 v3, v2
	v_mov_b32_e32 v4, v2
	v_mov_b32_e32 v5, v2
	v_mov_b32_e32 v6, v2
	v_mov_b32_e32 v7, v2
	v_mov_b32_e32 v8, v2
	v_mov_b32_e32 v9, v2
	v_mov_b32_e32 v10, v2
	v_mov_b32_e32 v11, v2
	v_mov_b32_e32 v12, v2
	v_mov_b32_e32 v13, v2
	v_mov_b32_e32 v14, v2
	v_mov_b32_e32 v15, v2
	v_mov_b32_e32 v16, v2
	v_mov_b32_e32 v17, v2
	s_waitcnt vmcnt(0)
	v_fma_mix_f32 v19, v124, v124, 0 op_sel_hi:[1,1,0]
	v_fma_mix_f32 v20, v120, v120, 0 op_sel_hi:[1,1,0]
	v_fma_mix_f32 v21, v116, v116, 0 op_sel_hi:[1,1,0]
	v_fma_mix_f32 v22, v112, v112, 0 op_sel_hi:[1,1,0]
	v_fma_mix_f32 v19, v124, v124, v19 op_sel:[1,1,0] op_sel_hi:[1,1,0]
	v_fma_mix_f32 v20, v120, v120, v20 op_sel:[1,1,0] op_sel_hi:[1,1,0]
	v_fma_mix_f32 v21, v116, v116, v21 op_sel:[1,1,0] op_sel_hi:[1,1,0]
	v_fma_mix_f32 v22, v112, v112, v22 op_sel:[1,1,0] op_sel_hi:[1,1,0]
	v_fma_mix_f32 v19, v125, v125, v19 op_sel_hi:[1,1,0]
	v_fma_mix_f32 v20, v121, v121, v20 op_sel_hi:[1,1,0]
	v_fma_mix_f32 v21, v117, v117, v21 op_sel_hi:[1,1,0]
	v_fma_mix_f32 v22, v113, v113, v22 op_sel_hi:[1,1,0]
	v_fma_mix_f32 v19, v125, v125, v19 op_sel:[1,1,0] op_sel_hi:[1,1,0]
	v_fma_mix_f32 v20, v121, v121, v20 op_sel:[1,1,0] op_sel_hi:[1,1,0]
	v_fma_mix_f32 v21, v117, v117, v21 op_sel:[1,1,0] op_sel_hi:[1,1,0]
	v_fma_mix_f32 v22, v113, v113, v22 op_sel:[1,1,0] op_sel_hi:[1,1,0]
	v_fma_mix_f32 v19, v126, v126, v19 op_sel_hi:[1,1,0]
	v_fma_mix_f32 v20, v122, v122, v20 op_sel_hi:[1,1,0]
	v_fma_mix_f32 v21, v118, v118, v21 op_sel_hi:[1,1,0]
	v_fma_mix_f32 v22, v114, v114, v22 op_sel_hi:[1,1,0]
	v_fma_mix_f32 v19, v126, v126, v19 op_sel:[1,1,0] op_sel_hi:[1,1,0]
	v_fma_mix_f32 v20, v122, v122, v20 op_sel:[1,1,0] op_sel_hi:[1,1,0]
	v_fma_mix_f32 v21, v118, v118, v21 op_sel:[1,1,0] op_sel_hi:[1,1,0]
	v_fma_mix_f32 v22, v114, v114, v22 op_sel:[1,1,0] op_sel_hi:[1,1,0]
	v_fma_mix_f32 v19, v127, v127, v19 op_sel_hi:[1,1,0]
	v_fma_mix_f32 v20, v123, v123, v20 op_sel_hi:[1,1,0]
	v_fma_mix_f32 v21, v119, v119, v21 op_sel_hi:[1,1,0]
	v_fma_mix_f32 v22, v115, v115, v22 op_sel_hi:[1,1,0]
	v_fma_mix_f32 v19, v127, v127, v19 op_sel:[1,1,0] op_sel_hi:[1,1,0]
	v_fma_mix_f32 v20, v123, v123, v20 op_sel:[1,1,0] op_sel_hi:[1,1,0]
	v_fma_mix_f32 v21, v119, v119, v21 op_sel:[1,1,0] op_sel_hi:[1,1,0]
	v_fma_mix_f32 v22, v115, v115, v22 op_sel:[1,1,0] op_sel_hi:[1,1,0]
	v_add_f32_e32 v19, v19, v20
	v_add_f32_e32 v21, v21, v22
	s_nop 0
	v_add_f32_e32 v19, v19, v21
	s_nop 0
	v_mov_b32_e32 v20, v19
	s_nop 1
	v_permlane32_swap_b32_e32 v19, v20
	v_add_f32_e32 v19, v19, v20
	s_waitcnt lgkmcnt(0)
	v_mul_f32_e32 v19, s5, v19
	v_cmp_ge_f32_e32 vcc, s4, v19
	s_cmp_eq_u64 vcc, exec
	s_cselect_b64 s[4:5], -1, 0
	s_add_u32 s6, s14, 0x4000
	s_addc_u32 s7, s15, 0
	s_add_i32 s10, s24, 0x4000
	s_mov_b32 s11, m0
	s_mov_b32 m0, s10
	s_nop 0
	global_load_lds_dwordx4 v189, s[6:7]
	s_mov_b32 m0, s11
	s_waitcnt vmcnt(3) lgkmcnt(0)
	s_barrier
	ds_read_b128 v[20:23], v190
	ds_read_b128 v[24:27], v190 offset:512
	s_waitcnt lgkmcnt(1)
	v_mfma_f32_32x32x16_f16 v[96:111], v[20:23], v[124:127], v[2:17]
	v_cndmask_b32_e64 v19, 0, 1, s[4:5]
	s_nop 0
	v_readfirstlane_b32 s4, v19
	s_bitcmp1_b32 s4, 0
	s_cselect_b64 s[16:17], -1, 0
	s_xor_b64 s[18:19], s[16:17], -1
	s_mov_b64 s[4:5], -1
	s_waitcnt lgkmcnt(0)
	v_mfma_f32_32x32x16_f16 v[80:95], v[24:27], v[124:127], v[2:17]
	ds_read_b128 v[20:23], v190 offset:2048
	ds_read_b128 v[24:27], v190 offset:2560
	s_and_b64 vcc, exec, s[18:19]
	s_waitcnt lgkmcnt(1)
	v_mfma_f32_32x32x16_f16 v[96:111], v[20:23], v[120:123], v[96:111]
	s_waitcnt lgkmcnt(0)
	v_mfma_f32_32x32x16_f16 v[80:95], v[24:27], v[120:123], v[80:95]
	ds_read_b128 v[20:23], v190 offset:4096
	ds_read_b128 v[24:27], v190 offset:4608
	s_waitcnt lgkmcnt(1)
	v_mfma_f32_32x32x16_f16 v[96:111], v[20:23], v[116:119], v[96:111]
	s_waitcnt lgkmcnt(0)
	v_mfma_f32_32x32x16_f16 v[80:95], v[24:27], v[116:119], v[80:95]
	ds_read_b128 v[20:23], v190 offset:6144
	ds_read_b128 v[24:27], v190 offset:6656
	s_waitcnt lgkmcnt(1)
	v_mfma_f32_32x32x16_f16 v[96:111], v[20:23], v[112:115], v[96:111]
	s_waitcnt lgkmcnt(0)
	v_mfma_f32_32x32x16_f16 v[80:95], v[24:27], v[112:115], v[80:95]
	s_cbranch_vccz .LBB2_2
	v_max3_f32 v19, v96, v97, v80
	v_max3_f32 v20, v98, v99, v81
	s_nop 0
	v_max3_f32 v19, v19, v82, v83
	v_max3_f32 v20, v20, v102, v103
	s_nop 0
	v_max3_f32 v19, v19, v100, v101
	v_max3_f32 v20, v20, v86, v87
	s_nop 0
	v_max3_f32 v19, v19, v84, v85
	v_max3_f32 v20, v20, v106, v107
	s_nop 0
	v_max3_f32 v19, v19, v104, v105
	v_max3_f32 v20, v20, v90, v91
	s_nop 0
	v_max3_f32 v19, v19, v88, v89
	v_max3_f32 v20, v20, v110, v111
	s_nop 0
	v_max3_f32 v19, v19, v108, v109
	v_max3_f32 v20, v20, v94, v95
	s_nop 0
	v_max3_f32 v19, v19, v92, v93
	s_nop 0
	v_max_f32 v19, v19, v20
	s_nop 0
	v_mov_b32_e32 v20, v19
	s_nop 1
	v_permlane32_swap_b32_e32 v19, v20
	v_max_f32 v180, v19, v20
	s_nop 0
	v_sub_f32_e32 v19, v96, v180
	v_exp_f32_e32 v64, v19
	v_sub_f32_e32 v19, v80, v180
	v_exp_f32_e32 v48, v19
	v_sub_f32_e32 v19, v97, v180
	v_exp_f32_e32 v65, v19
	v_sub_f32_e32 v19, v81, v180
	v_exp_f32_e32 v49, v19
	v_sub_f32_e32 v19, v98, v180
	v_exp_f32_e32 v66, v19
	v_sub_f32_e32 v19, v82, v180
	v_exp_f32_e32 v50, v19
	v_sub_f32_e32 v19, v99, v180
	v_exp_f32_e32 v67, v19
	v_sub_f32_e32 v19, v83, v180
	v_exp_f32_e32 v51, v19
	v_sub_f32_e32 v19, v100, v180
	v_exp_f32_e32 v68, v19
	v_sub_f32_e32 v19, v84, v180
	v_exp_f32_e32 v52, v19
	v_sub_f32_e32 v19, v101, v180
	v_exp_f32_e32 v69, v19
	v_sub_f32_e32 v19, v85, v180
	v_exp_f32_e32 v53, v19
	v_sub_f32_e32 v19, v102, v180
	v_exp_f32_e32 v70, v19
	v_sub_f32_e32 v19, v86, v180
	v_exp_f32_e32 v54, v19
	v_sub_f32_e32 v19, v103, v180
	v_exp_f32_e32 v71, v19
	v_sub_f32_e32 v19, v87, v180
	v_exp_f32_e32 v55, v19
	v_sub_f32_e32 v19, v104, v180
	v_exp_f32_e32 v72, v19
	v_sub_f32_e32 v19, v105, v180
	v_exp_f32_e32 v73, v19
	v_sub_f32_e32 v19, v106, v180
	v_exp_f32_e32 v74, v19
	v_sub_f32_e32 v19, v107, v180
	v_exp_f32_e32 v75, v19
	v_sub_f32_e32 v19, v108, v180
	v_exp_f32_e32 v76, v19
	v_sub_f32_e32 v19, v109, v180
	v_exp_f32_e32 v77, v19
	v_sub_f32_e32 v19, v110, v180
	v_xor_b32_e32 v32, 0x80000000, v180
	v_exp_f32_e32 v78, v19
	v_sub_f32_e32 v19, v111, v180
	v_mov_b32_e32 v33, v32
	v_mov_b32_e32 v34, v32
	v_mov_b32_e32 v35, v32
	v_mov_b32_e32 v36, v32
	v_mov_b32_e32 v37, v32
	v_mov_b32_e32 v38, v32
	v_mov_b32_e32 v39, v32
	v_mov_b32_e32 v40, v32
	v_mov_b32_e32 v41, v32
	v_mov_b32_e32 v42, v32
	v_mov_b32_e32 v43, v32
	v_mov_b32_e32 v44, v32
	v_mov_b32_e32 v45, v32
	v_mov_b32_e32 v46, v32
	v_mov_b32_e32 v47, v32
	v_pk_add_f32 v[56:57], v[88:89], v[180:181] op_sel_hi:[1,0] neg_lo:[0,1] neg_hi:[0,1]
	v_pk_add_f32 v[58:59], v[90:91], v[180:181] op_sel_hi:[1,0] neg_lo:[0,1] neg_hi:[0,1]
	v_pk_add_f32 v[60:61], v[92:93], v[180:181] op_sel_hi:[1,0] neg_lo:[0,1] neg_hi:[0,1]
	v_exp_f32_e32 v79, v19
	v_pk_add_f32 v[62:63], v[94:95], v[180:181] op_sel_hi:[1,0] neg_lo:[0,1] neg_hi:[0,1]
	s_load_dwordx2 s[6:7], s[0:1], 0x20
	s_lshl_b32 s21, s27, 6
	s_cbranch_execz .LBB2_3
	s_branch .LBB2_4
